# baseline (speedup 1.0000x reference)
.LBB1_33:
	v_lshl_or_b32 v150, v202, 6, s20
	v_mov_b32_e32 v151, s21
	v_or_b32_e32 v152, v204, v203
	v_lshlrev_b64 v[150:151], 10, v[150:151]
	v_add_u32_e32 v152, s34, v152
	v_or_b32_e32 v150, v150, v152
	v_cndmask_b32_e64 v152, v160, v156, s[0:1]
	v_cndmask_b32_e64 v130, v161, v130, s[0:1]
	v_add_f32_e32 v152, v152, v154
	v_add_f32_e32 v130, v130, v155
	v_mul_f32_e32 v133, v152, v133
	v_mul_f32_e32 v146, v152, v146
	v_fmac_f32_e32 v133, v130, v147
	v_fmac_f32_e32 v146, v130, v132
	v_cndmask_b32_e64 v148, v148, 0, s[0:1]
	v_cndmask_b32_e64 v149, v149, 0, s[0:1]
	v_cndmask_b32_e64 v130, v133, v130, s[0:1]
	v_cndmask_b32_e64 v132, v146, v152, s[0:1]
	v_add_f32_e32 v152, v130, v148
	v_add_f32_e32 v130, v132, v149
	ds_bpermute_b32 v226, v0, v145
	ds_bpermute_b32 v231, v0, v144
	s_waitcnt lgkmcnt(1)
	v_cndmask_b32_e64 v225, v226, v145, s[0:1]
	s_andn2_b64 vcc, exec, s[6:7]
	s_waitcnt lgkmcnt(0)
	v_cndmask_b32_e64 v224, v231, v144, s[0:1]
	s_cbranch_vccnz .Lmg_np
.Lmg_pow:
	v_pk_mul_f32 v[228:229], v[224:225], v[140:141] op_sel:[1,0] op_sel_hi:[0,1]
	s_add_i32 s8, s8, -1
	s_cmp_lg_u32 s8, 0
	v_pk_fma_f32 v[224:225], v[224:225], v[142:143], v[228:229]
	s_cbranch_scc1 .Lmg_pow
.Lmg_np:
	v_cndmask_b32_e64 v227, v145, v226, s[0:1]
	v_cndmask_b32_e64 v226, v144, v231, s[0:1]
	v_pk_add_f32 v[224:225], v[226:227], v[224:225]
	v_cndmask_b32_e64 v230, v135, 0, s[0:1]
	v_pk_mul_f32 v[228:229], v[224:225], v[138:139] op_sel:[1,0] op_sel_hi:[0,1]
	v_pk_mov_b32 v[226:227], v[224:225], v[224:225] op_sel:[1,0]
	v_pk_fma_f32 v[224:225], v[224:225], v[136:137], v[228:229]
	v_cndmask_b32_e64 v228, v134, 0, s[0:1]
	v_cndmask_b32_e64 v224, v224, v226, s[0:1]
	v_cndmask_b32_e64 v225, v225, v227, s[0:1]
	v_add_f32_e32 v230, v224, v230
	v_add_f32_e32 v228, v225, v228
	v_lshlrev_b32_e32 v232, 2, v150
	s_add_u32 s44, s18, 0x4000000
	s_addc_u32 s45, s19, 0
	s_add_u32 s46, s18, 0x8000000
	s_addc_u32 s47, s19, 0
	s_mov_b32 s48, 0x3dcccccd
	v_mov_b32_e32 v235, v232
	v_mov_b32_e32 v236, v232
	v_mov_b32_e32 v237, v232
	v_fma_f32 v233, -v130, v131, v82
	v_fmac_f32_e32 v152, 0x3dcccccd, v233
	v_fma_f32 v82, s48, v152, v130
	global_store_dword v232, v82, s[18:19]
	v_add_u32_e32 v232, 0x1000, v232
	global_store_dword v235, v152, s[44:45]
	v_add_u32_e32 v235, 0x1000, v235
	global_store_dword v236, v82, s[46:47]
	v_add_u32_e32 v236, 0x1000, v236
	v_fma_f32 v233, -v82, v131, v83
	v_fmac_f32_e32 v152, 0x3dcccccd, v233
	v_fma_f32 v83, s48, v152, v82
	global_store_dword v232, v83, s[18:19]
	v_add_u32_e32 v232, 0x1000, v232
	global_store_dword v235, v152, s[44:45]
	v_add_u32_e32 v235, 0x1000, v235
	global_store_dword v236, v83, s[46:47]
	v_add_u32_e32 v236, 0x1000, v236
	v_fma_f32 v233, -v83, v131, v84
	v_fmac_f32_e32 v152, 0x3dcccccd, v233
	v_fma_f32 v84, s48, v152, v83
	global_store_dword v232, v84, s[18:19]
	v_add_u32_e32 v232, 0x1000, v232
	global_store_dword v235, v152, s[44:45]
	v_add_u32_e32 v235, 0x1000, v235
	global_store_dword v236, v84, s[46:47]
	v_add_u32_e32 v236, 0x1000, v236
	v_fma_f32 v233, -v84, v131, v85
	v_fmac_f32_e32 v152, 0x3dcccccd, v233
	v_fma_f32 v85, s48, v152, v84
	global_store_dword v232, v85, s[18:19]
	v_add_u32_e32 v232, 0x1000, v232
	global_store_dword v235, v152, s[44:45]
	v_add_u32_e32 v235, 0x1000, v235
	global_store_dword v236, v85, s[46:47]
	v_add_u32_e32 v236, 0x1000, v236
	v_fma_f32 v233, -v85, v131, v86
	v_fmac_f32_e32 v152, 0x3dcccccd, v233
	v_fma_f32 v86, s48, v152, v85
	global_store_dword v232, v86, s[18:19]
	v_add_u32_e32 v232, 0x1000, v232
	global_store_dword v235, v152, s[44:45]
	v_add_u32_e32 v235, 0x1000, v235
	global_store_dword v236, v86, s[46:47]
	v_add_u32_e32 v236, 0x1000, v236
	v_fma_f32 v233, -v86, v131, v87
	v_fmac_f32_e32 v152, 0x3dcccccd, v233
	v_fma_f32 v87, s48, v152, v86
	global_store_dword v232, v87, s[18:19]
	v_add_u32_e32 v232, 0x1000, v232
	global_store_dword v235, v152, s[44:45]
	v_add_u32_e32 v235, 0x1000, v235
	global_store_dword v236, v87, s[46:47]
	v_add_u32_e32 v236, 0x1000, v236
	v_fma_f32 v233, -v87, v131, v88
	v_fmac_f32_e32 v152, 0x3dcccccd, v233
	v_fma_f32 v88, s48, v152, v87
	global_store_dword v232, v88, s[18:19]
	v_add_u32_e32 v232, 0x1000, v232
	global_store_dword v235, v152, s[44:45]
	v_add_u32_e32 v235, 0x1000, v235
	global_store_dword v236, v88, s[46:47]
	v_add_u32_e32 v236, 0x1000, v236
	v_fma_f32 v233, -v88, v131, v89
	v_fmac_f32_e32 v152, 0x3dcccccd, v233
	v_fma_f32 v89, s48, v152, v88
	global_store_dword v232, v89, s[18:19]
	v_add_u32_e32 v232, 0x1000, v232
	global_store_dword v235, v152, s[44:45]
	v_add_u32_e32 v235, 0x1000, v235
	global_store_dword v236, v89, s[46:47]
	v_add_u32_e32 v236, 0x1000, v236
	v_fma_f32 v233, -v89, v131, v90
	v_fmac_f32_e32 v152, 0x3dcccccd, v233
	v_fma_f32 v90, s48, v152, v89
	global_store_dword v232, v90, s[18:19]
	v_add_u32_e32 v232, 0x1000, v232
	global_store_dword v235, v152, s[44:45]
	v_add_u32_e32 v235, 0x1000, v235
	global_store_dword v236, v90, s[46:47]
	v_add_u32_e32 v236, 0x1000, v236
	v_fma_f32 v233, -v90, v131, v91
	v_fmac_f32_e32 v152, 0x3dcccccd, v233
	v_fma_f32 v91, s48, v152, v90
	global_store_dword v232, v91, s[18:19]
	v_add_u32_e32 v232, 0x1000, v232
	global_store_dword v235, v152, s[44:45]
	v_add_u32_e32 v235, 0x1000, v235
	global_store_dword v236, v91, s[46:47]
	v_add_u32_e32 v236, 0x1000, v236
	v_fma_f32 v233, -v91, v131, v92
	v_fmac_f32_e32 v152, 0x3dcccccd, v233
	v_fma_f32 v92, s48, v152, v91
	global_store_dword v232, v92, s[18:19]
	v_add_u32_e32 v232, 0x1000, v232
	global_store_dword v235, v152, s[44:45]
	v_add_u32_e32 v235, 0x1000, v235
	global_store_dword v236, v92, s[46:47]
	v_add_u32_e32 v236, 0x1000, v236
	v_fma_f32 v233, -v92, v131, v93
	v_fmac_f32_e32 v152, 0x3dcccccd, v233
	v_fma_f32 v93, s48, v152, v92
	global_store_dword v232, v93, s[18:19]
	v_add_u32_e32 v232, 0x1000, v232
	global_store_dword v235, v152, s[44:45]
	v_add_u32_e32 v235, 0x1000, v235
	global_store_dword v236, v93, s[46:47]
	v_add_u32_e32 v236, 0x1000, v236
	v_fma_f32 v233, -v93, v131, v94
	v_fmac_f32_e32 v152, 0x3dcccccd, v233
	v_fma_f32 v94, s48, v152, v93
	global_store_dword v232, v94, s[18:19]
	v_add_u32_e32 v232, 0x1000, v232
	global_store_dword v235, v152, s[44:45]
	v_add_u32_e32 v235, 0x1000, v235
	global_store_dword v236, v94, s[46:47]
	v_add_u32_e32 v236, 0x1000, v236
	v_fma_f32 v233, -v94, v131, v95
	v_fmac_f32_e32 v152, 0x3dcccccd, v233
	v_fma_f32 v95, s48, v152, v94
	global_store_dword v232, v95, s[18:19]
	v_add_u32_e32 v232, 0x1000, v232
	global_store_dword v235, v152, s[44:45]
	v_add_u32_e32 v235, 0x1000, v235
	global_store_dword v236, v95, s[46:47]
	v_add_u32_e32 v236, 0x1000, v236
	v_fma_f32 v233, -v95, v131, v96
	v_fmac_f32_e32 v152, 0x3dcccccd, v233
	v_fma_f32 v96, s48, v152, v95
	global_store_dword v232, v96, s[18:19]
	v_add_u32_e32 v232, 0x1000, v232
	global_store_dword v235, v152, s[44:45]
	v_add_u32_e32 v235, 0x1000, v235
	global_store_dword v236, v96, s[46:47]
	v_add_u32_e32 v236, 0x1000, v236
	v_fma_f32 v233, -v96, v131, v97
	v_fmac_f32_e32 v152, 0x3dcccccd, v233
	v_fma_f32 v97, s48, v152, v96
	global_store_dword v232, v97, s[18:19]
	v_add_u32_e32 v232, 0x1000, v232
	global_store_dword v235, v152, s[44:45]
	v_add_u32_e32 v235, 0x1000, v235
	global_store_dword v236, v97, s[46:47]
	v_add_u32_e32 v236, 0x1000, v236
	v_fma_f32 v233, -v97, v131, v114
	v_fmac_f32_e32 v152, 0x3dcccccd, v233
	v_fma_f32 v114, s48, v152, v97
	global_store_dword v232, v114, s[18:19]
	v_add_u32_e32 v232, 0x1000, v232
	global_store_dword v235, v152, s[44:45]
	v_add_u32_e32 v235, 0x1000, v235
	global_store_dword v236, v114, s[46:47]
	v_add_u32_e32 v236, 0x1000, v236
	v_fma_f32 v233, -v114, v131, v115
	v_fmac_f32_e32 v152, 0x3dcccccd, v233
	v_fma_f32 v115, s48, v152, v114
	global_store_dword v232, v115, s[18:19]
	v_add_u32_e32 v232, 0x1000, v232
	global_store_dword v235, v152, s[44:45]
	v_add_u32_e32 v235, 0x1000, v235
	global_store_dword v236, v115, s[46:47]
	v_add_u32_e32 v236, 0x1000, v236
	v_fma_f32 v233, -v115, v131, v116
	v_fmac_f32_e32 v152, 0x3dcccccd, v233
	v_fma_f32 v116, s48, v152, v115
	global_store_dword v232, v116, s[18:19]
	v_add_u32_e32 v232, 0x1000, v232
	global_store_dword v235, v152, s[44:45]
	v_add_u32_e32 v235, 0x1000, v235
	global_store_dword v236, v116, s[46:47]
	v_add_u32_e32 v236, 0x1000, v236
	v_fma_f32 v233, -v116, v131, v117
	v_fmac_f32_e32 v152, 0x3dcccccd, v233
	v_fma_f32 v117, s48, v152, v116
	global_store_dword v232, v117, s[18:19]
	v_add_u32_e32 v232, 0x1000, v232
	global_store_dword v235, v152, s[44:45]
	v_add_u32_e32 v235, 0x1000, v235
	global_store_dword v236, v117, s[46:47]
	v_add_u32_e32 v236, 0x1000, v236
	v_fma_f32 v233, -v117, v131, v118
	v_fmac_f32_e32 v152, 0x3dcccccd, v233
	v_fma_f32 v118, s48, v152, v117
	global_store_dword v232, v118, s[18:19]
	v_add_u32_e32 v232, 0x1000, v232
	global_store_dword v235, v152, s[44:45]
	v_add_u32_e32 v235, 0x1000, v235
	global_store_dword v236, v118, s[46:47]
	v_add_u32_e32 v236, 0x1000, v236
	v_fma_f32 v233, -v118, v131, v119
	v_fmac_f32_e32 v152, 0x3dcccccd, v233
	v_fma_f32 v119, s48, v152, v118
	global_store_dword v232, v119, s[18:19]
	v_add_u32_e32 v232, 0x1000, v232
	global_store_dword v235, v152, s[44:45]
	v_add_u32_e32 v235, 0x1000, v235
	global_store_dword v236, v119, s[46:47]
	v_add_u32_e32 v236, 0x1000, v236
	v_fma_f32 v233, -v119, v131, v120
	v_fmac_f32_e32 v152, 0x3dcccccd, v233
	v_fma_f32 v120, s48, v152, v119
	global_store_dword v232, v120, s[18:19]
	v_add_u32_e32 v232, 0x1000, v232
	global_store_dword v235, v152, s[44:45]
	v_add_u32_e32 v235, 0x1000, v235
	global_store_dword v236, v120, s[46:47]
	v_add_u32_e32 v236, 0x1000, v236
	v_fma_f32 v233, -v120, v131, v121
	v_fmac_f32_e32 v152, 0x3dcccccd, v233
	v_fma_f32 v121, s48, v152, v120
	global_store_dword v232, v121, s[18:19]
	v_add_u32_e32 v232, 0x1000, v232
	global_store_dword v235, v152, s[44:45]
	v_add_u32_e32 v235, 0x1000, v235
	global_store_dword v236, v121, s[46:47]
	v_add_u32_e32 v236, 0x1000, v236
	v_fma_f32 v233, -v121, v131, v122
	v_fmac_f32_e32 v152, 0x3dcccccd, v233
	v_fma_f32 v122, s48, v152, v121
	global_store_dword v232, v122, s[18:19]
	v_add_u32_e32 v232, 0x1000, v232
	global_store_dword v235, v152, s[44:45]
	v_add_u32_e32 v235, 0x1000, v235
	global_store_dword v236, v122, s[46:47]
	v_add_u32_e32 v236, 0x1000, v236
	v_fma_f32 v233, -v122, v131, v123
	v_fmac_f32_e32 v152, 0x3dcccccd, v233
	v_fma_f32 v123, s48, v152, v122
	global_store_dword v232, v123, s[18:19]
	v_add_u32_e32 v232, 0x1000, v232
	global_store_dword v235, v152, s[44:45]
	v_add_u32_e32 v235, 0x1000, v235
	global_store_dword v236, v123, s[46:47]
	v_add_u32_e32 v236, 0x1000, v236
	v_fma_f32 v233, -v123, v131, v124
	v_fmac_f32_e32 v152, 0x3dcccccd, v233
	v_fma_f32 v124, s48, v152, v123
	global_store_dword v232, v124, s[18:19]
	v_add_u32_e32 v232, 0x1000, v232
	global_store_dword v235, v152, s[44:45]
	v_add_u32_e32 v235, 0x1000, v235
	global_store_dword v236, v124, s[46:47]
	v_add_u32_e32 v236, 0x1000, v236
	v_fma_f32 v233, -v124, v131, v125
	v_fmac_f32_e32 v152, 0x3dcccccd, v233
	v_fma_f32 v125, s48, v152, v124
	global_store_dword v232, v125, s[18:19]
	v_add_u32_e32 v232, 0x1000, v232
	global_store_dword v235, v152, s[44:45]
	v_add_u32_e32 v235, 0x1000, v235
	global_store_dword v236, v125, s[46:47]
	v_add_u32_e32 v236, 0x1000, v236
	v_fma_f32 v233, -v125, v131, v126
	v_fmac_f32_e32 v152, 0x3dcccccd, v233
	v_fma_f32 v126, s48, v152, v125
	global_store_dword v232, v126, s[18:19]
	v_add_u32_e32 v232, 0x1000, v232
	global_store_dword v235, v152, s[44:45]
	v_add_u32_e32 v235, 0x1000, v235
	global_store_dword v236, v126, s[46:47]
	v_add_u32_e32 v236, 0x1000, v236
	v_fma_f32 v233, -v126, v131, v127
	v_fmac_f32_e32 v152, 0x3dcccccd, v233
	v_fma_f32 v127, s48, v152, v126
	global_store_dword v232, v127, s[18:19]
	v_add_u32_e32 v232, 0x1000, v232
	global_store_dword v235, v152, s[44:45]
	v_add_u32_e32 v235, 0x1000, v235
	global_store_dword v236, v127, s[46:47]
	v_add_u32_e32 v236, 0x1000, v236
	v_fma_f32 v233, -v127, v131, v128
	v_fmac_f32_e32 v152, 0x3dcccccd, v233
	v_fma_f32 v128, s48, v152, v127
	global_store_dword v232, v128, s[18:19]
	v_add_u32_e32 v232, 0x1000, v232
	global_store_dword v235, v152, s[44:45]
	v_add_u32_e32 v235, 0x1000, v235
	global_store_dword v236, v128, s[46:47]
	v_add_u32_e32 v236, 0x1000, v236
	v_fma_f32 v233, -v128, v131, v129
	v_fmac_f32_e32 v152, 0x3dcccccd, v233
	v_fma_f32 v129, s48, v152, v128
	global_store_dword v232, v129, s[18:19]
	v_add_u32_e32 v232, 0x1000, v232
	global_store_dword v235, v152, s[44:45]
	v_add_u32_e32 v235, 0x1000, v235
	global_store_dword v236, v129, s[46:47]
	v_add_u32_e32 v236, 0x1000, v236
	v_fma_f32 v233, -v129, v131, v98
	v_fmac_f32_e32 v152, 0x3dcccccd, v233
	v_fma_f32 v98, s48, v152, v129
	global_store_dword v232, v98, s[18:19]
	v_add_u32_e32 v232, 0x1000, v232
	global_store_dword v235, v152, s[44:45]
	v_add_u32_e32 v235, 0x1000, v235
	global_store_dword v236, v98, s[46:47]
	v_add_u32_e32 v236, 0x1000, v236
	v_fma_f32 v233, -v98, v131, v99
	v_fmac_f32_e32 v152, 0x3dcccccd, v233
	v_fma_f32 v99, s48, v152, v98
	global_store_dword v232, v99, s[18:19]
	v_add_u32_e32 v232, 0x1000, v232
	global_store_dword v235, v152, s[44:45]
	v_add_u32_e32 v235, 0x1000, v235
	global_store_dword v236, v99, s[46:47]
	v_add_u32_e32 v236, 0x1000, v236
	v_fma_f32 v233, -v99, v131, v100
	v_fmac_f32_e32 v152, 0x3dcccccd, v233
	v_fma_f32 v100, s48, v152, v99
	global_store_dword v232, v100, s[18:19]
	v_add_u32_e32 v232, 0x1000, v232
	global_store_dword v235, v152, s[44:45]
	v_add_u32_e32 v235, 0x1000, v235
	global_store_dword v236, v100, s[46:47]
	v_add_u32_e32 v236, 0x1000, v236
	v_fma_f32 v233, -v100, v131, v101
	v_fmac_f32_e32 v152, 0x3dcccccd, v233
	v_fma_f32 v101, s48, v152, v100
	global_store_dword v232, v101, s[18:19]
	v_add_u32_e32 v232, 0x1000, v232
	global_store_dword v235, v152, s[44:45]
	v_add_u32_e32 v235, 0x1000, v235
	global_store_dword v236, v101, s[46:47]
	v_add_u32_e32 v236, 0x1000, v236
	v_fma_f32 v233, -v101, v131, v102
	v_fmac_f32_e32 v152, 0x3dcccccd, v233
	v_fma_f32 v102, s48, v152, v101
	global_store_dword v232, v102, s[18:19]
	v_add_u32_e32 v232, 0x1000, v232
	global_store_dword v235, v152, s[44:45]
	v_add_u32_e32 v235, 0x1000, v235
	global_store_dword v236, v102, s[46:47]
	v_add_u32_e32 v236, 0x1000, v236
	v_fma_f32 v233, -v102, v131, v103
	v_fmac_f32_e32 v152, 0x3dcccccd, v233
	v_fma_f32 v103, s48, v152, v102
	global_store_dword v232, v103, s[18:19]
	v_add_u32_e32 v232, 0x1000, v232
	global_store_dword v235, v152, s[44:45]
	v_add_u32_e32 v235, 0x1000, v235
	global_store_dword v236, v103, s[46:47]
	v_add_u32_e32 v236, 0x1000, v236
	v_fma_f32 v233, -v103, v131, v104
	v_fmac_f32_e32 v152, 0x3dcccccd, v233
	v_fma_f32 v104, s48, v152, v103
	global_store_dword v232, v104, s[18:19]
	v_add_u32_e32 v232, 0x1000, v232
	global_store_dword v235, v152, s[44:45]
	v_add_u32_e32 v235, 0x1000, v235
	global_store_dword v236, v104, s[46:47]
	v_add_u32_e32 v236, 0x1000, v236
	v_fma_f32 v233, -v104, v131, v105
	v_fmac_f32_e32 v152, 0x3dcccccd, v233
	v_fma_f32 v105, s48, v152, v104
	global_store_dword v232, v105, s[18:19]
	v_add_u32_e32 v232, 0x1000, v232
	global_store_dword v235, v152, s[44:45]
	v_add_u32_e32 v235, 0x1000, v235
	global_store_dword v236, v105, s[46:47]
	v_add_u32_e32 v236, 0x1000, v236
	v_fma_f32 v233, -v105, v131, v106
	v_fmac_f32_e32 v152, 0x3dcccccd, v233
	v_fma_f32 v106, s48, v152, v105
	global_store_dword v232, v106, s[18:19]
	v_add_u32_e32 v232, 0x1000, v232
	global_store_dword v235, v152, s[44:45]
	v_add_u32_e32 v235, 0x1000, v235
	global_store_dword v236, v106, s[46:47]
	v_add_u32_e32 v236, 0x1000, v236
	v_fma_f32 v233, -v106, v131, v107
	v_fmac_f32_e32 v152, 0x3dcccccd, v233
	v_fma_f32 v107, s48, v152, v106
	global_store_dword v232, v107, s[18:19]
	v_add_u32_e32 v232, 0x1000, v232
	global_store_dword v235, v152, s[44:45]
	v_add_u32_e32 v235, 0x1000, v235
	global_store_dword v236, v107, s[46:47]
	v_add_u32_e32 v236, 0x1000, v236
	v_fma_f32 v233, -v107, v131, v108
	v_fmac_f32_e32 v152, 0x3dcccccd, v233
	v_fma_f32 v108, s48, v152, v107
	global_store_dword v232, v108, s[18:19]
	v_add_u32_e32 v232, 0x1000, v232
	global_store_dword v235, v152, s[44:45]
	v_add_u32_e32 v235, 0x1000, v235
	global_store_dword v236, v108, s[46:47]
	v_add_u32_e32 v236, 0x1000, v236
	v_fma_f32 v233, -v108, v131, v109
	v_fmac_f32_e32 v152, 0x3dcccccd, v233
	v_fma_f32 v109, s48, v152, v108
	global_store_dword v232, v109, s[18:19]
	v_add_u32_e32 v232, 0x1000, v232
	global_store_dword v235, v152, s[44:45]
	v_add_u32_e32 v235, 0x1000, v235
	global_store_dword v236, v109, s[46:47]
	v_add_u32_e32 v236, 0x1000, v236
	v_fma_f32 v233, -v109, v131, v110
	v_fmac_f32_e32 v152, 0x3dcccccd, v233
	v_fma_f32 v110, s48, v152, v109
	global_store_dword v232, v110, s[18:19]
	v_add_u32_e32 v232, 0x1000, v232
	global_store_dword v235, v152, s[44:45]
	v_add_u32_e32 v235, 0x1000, v235
	global_store_dword v236, v110, s[46:47]
	v_add_u32_e32 v236, 0x1000, v236
	v_fma_f32 v233, -v110, v131, v111
	v_fmac_f32_e32 v152, 0x3dcccccd, v233
	v_fma_f32 v111, s48, v152, v110
	global_store_dword v232, v111, s[18:19]
	v_add_u32_e32 v232, 0x1000, v232
	global_store_dword v235, v152, s[44:45]
	v_add_u32_e32 v235, 0x1000, v235
	global_store_dword v236, v111, s[46:47]
	v_add_u32_e32 v236, 0x1000, v236
	v_fma_f32 v233, -v111, v131, v112
	v_fmac_f32_e32 v152, 0x3dcccccd, v233
	v_fma_f32 v112, s48, v152, v111
	global_store_dword v232, v112, s[18:19]
	v_add_u32_e32 v232, 0x1000, v232
	global_store_dword v235, v152, s[44:45]
	v_add_u32_e32 v235, 0x1000, v235
	global_store_dword v236, v112, s[46:47]
	v_add_u32_e32 v236, 0x1000, v236
	v_fma_f32 v233, -v112, v131, v113
	v_fmac_f32_e32 v152, 0x3dcccccd, v233
	v_fma_f32 v113, s48, v152, v112
	global_store_dword v232, v113, s[18:19]
	v_add_u32_e32 v232, 0x1000, v232
	global_store_dword v235, v152, s[44:45]
	v_add_u32_e32 v235, 0x1000, v235
	global_store_dword v236, v113, s[46:47]
	v_add_u32_e32 v236, 0x1000, v236
	v_fma_f32 v233, -v113, v131, v66
	v_fmac_f32_e32 v152, 0x3dcccccd, v233
	v_fma_f32 v66, s48, v152, v113
	global_store_dword v232, v66, s[18:19]
	v_add_u32_e32 v232, 0x1000, v232
	global_store_dword v235, v152, s[44:45]
	v_add_u32_e32 v235, 0x1000, v235
	global_store_dword v236, v66, s[46:47]
	v_add_u32_e32 v236, 0x1000, v236
	v_fma_f32 v233, -v66, v131, v67
	v_fmac_f32_e32 v152, 0x3dcccccd, v233
	v_fma_f32 v67, s48, v152, v66
	global_store_dword v232, v67, s[18:19]
	v_add_u32_e32 v232, 0x1000, v232
	global_store_dword v235, v152, s[44:45]
	v_add_u32_e32 v235, 0x1000, v235
	global_store_dword v236, v67, s[46:47]
	v_add_u32_e32 v236, 0x1000, v236
	v_fma_f32 v233, -v67, v131, v68
	v_fmac_f32_e32 v152, 0x3dcccccd, v233
	v_fma_f32 v68, s48, v152, v67
	global_store_dword v232, v68, s[18:19]
	v_add_u32_e32 v232, 0x1000, v232
	global_store_dword v235, v152, s[44:45]
	v_add_u32_e32 v235, 0x1000, v235
	global_store_dword v236, v68, s[46:47]
	v_add_u32_e32 v236, 0x1000, v236
	v_fma_f32 v233, -v68, v131, v69
	v_fmac_f32_e32 v152, 0x3dcccccd, v233
	v_fma_f32 v69, s48, v152, v68
	global_store_dword v232, v69, s[18:19]
	v_add_u32_e32 v232, 0x1000, v232
	global_store_dword v235, v152, s[44:45]
	v_add_u32_e32 v235, 0x1000, v235
	global_store_dword v236, v69, s[46:47]
	v_add_u32_e32 v236, 0x1000, v236
	v_fma_f32 v233, -v69, v131, v70
	v_fmac_f32_e32 v152, 0x3dcccccd, v233
	v_fma_f32 v70, s48, v152, v69
	global_store_dword v232, v70, s[18:19]
	v_add_u32_e32 v232, 0x1000, v232
	global_store_dword v235, v152, s[44:45]
	v_add_u32_e32 v235, 0x1000, v235
	global_store_dword v236, v70, s[46:47]
	v_add_u32_e32 v236, 0x1000, v236
	v_fma_f32 v233, -v70, v131, v71
	v_fmac_f32_e32 v152, 0x3dcccccd, v233
	v_fma_f32 v71, s48, v152, v70
	global_store_dword v232, v71, s[18:19]
	v_add_u32_e32 v232, 0x1000, v232
	global_store_dword v235, v152, s[44:45]
	v_add_u32_e32 v235, 0x1000, v235
	global_store_dword v236, v71, s[46:47]
	v_add_u32_e32 v236, 0x1000, v236
	v_fma_f32 v233, -v71, v131, v72
	v_fmac_f32_e32 v152, 0x3dcccccd, v233
	v_fma_f32 v72, s48, v152, v71
	global_store_dword v232, v72, s[18:19]
	v_add_u32_e32 v232, 0x1000, v232
	global_store_dword v235, v152, s[44:45]
	v_add_u32_e32 v235, 0x1000, v235
	global_store_dword v236, v72, s[46:47]
	v_add_u32_e32 v236, 0x1000, v236
	v_fma_f32 v233, -v72, v131, v73
	v_fmac_f32_e32 v152, 0x3dcccccd, v233
	v_fma_f32 v73, s48, v152, v72
	global_store_dword v232, v73, s[18:19]
	v_add_u32_e32 v232, 0x1000, v232
	global_store_dword v235, v152, s[44:45]
	v_add_u32_e32 v235, 0x1000, v235
	global_store_dword v236, v73, s[46:47]
	v_add_u32_e32 v236, 0x1000, v236
	v_fma_f32 v233, -v73, v131, v74
	v_fmac_f32_e32 v152, 0x3dcccccd, v233
	v_fma_f32 v74, s48, v152, v73
	global_store_dword v232, v74, s[18:19]
	v_add_u32_e32 v232, 0x1000, v232
	global_store_dword v235, v152, s[44:45]
	v_add_u32_e32 v235, 0x1000, v235
	global_store_dword v236, v74, s[46:47]
	v_add_u32_e32 v236, 0x1000, v236
	v_fma_f32 v233, -v74, v131, v75
	v_fmac_f32_e32 v152, 0x3dcccccd, v233
	v_fma_f32 v75, s48, v152, v74
	global_store_dword v232, v75, s[18:19]
	v_add_u32_e32 v232, 0x1000, v232
	global_store_dword v235, v152, s[44:45]
	v_add_u32_e32 v235, 0x1000, v235
	global_store_dword v236, v75, s[46:47]
	v_add_u32_e32 v236, 0x1000, v236
	v_fma_f32 v233, -v75, v131, v76
	v_fmac_f32_e32 v152, 0x3dcccccd, v233
	v_fma_f32 v76, s48, v152, v75
	global_store_dword v232, v76, s[18:19]
	v_add_u32_e32 v232, 0x1000, v232
	global_store_dword v235, v152, s[44:45]
	v_add_u32_e32 v235, 0x1000, v235
	global_store_dword v236, v76, s[46:47]
	v_add_u32_e32 v236, 0x1000, v236
	v_fma_f32 v233, -v76, v131, v77
	v_fmac_f32_e32 v152, 0x3dcccccd, v233
	v_fma_f32 v77, s48, v152, v76
	global_store_dword v232, v77, s[18:19]
	v_add_u32_e32 v232, 0x1000, v232
	global_store_dword v235, v152, s[44:45]
	v_add_u32_e32 v235, 0x1000, v235
	global_store_dword v236, v77, s[46:47]
	v_add_u32_e32 v236, 0x1000, v236
	v_fma_f32 v233, -v77, v131, v78
	v_fmac_f32_e32 v152, 0x3dcccccd, v233
	v_fma_f32 v78, s48, v152, v77
	global_store_dword v232, v78, s[18:19]
	v_add_u32_e32 v232, 0x1000, v232
	global_store_dword v235, v152, s[44:45]
	v_add_u32_e32 v235, 0x1000, v235
	global_store_dword v236, v78, s[46:47]
	v_add_u32_e32 v236, 0x1000, v236
	v_fma_f32 v233, -v78, v131, v79
	v_fmac_f32_e32 v152, 0x3dcccccd, v233
	v_fma_f32 v79, s48, v152, v78
	global_store_dword v232, v79, s[18:19]
	v_add_u32_e32 v232, 0x1000, v232
	global_store_dword v235, v152, s[44:45]
	v_add_u32_e32 v235, 0x1000, v235
	global_store_dword v236, v79, s[46:47]
	v_add_u32_e32 v236, 0x1000, v236
	v_fma_f32 v233, -v79, v131, v80
	v_fmac_f32_e32 v152, 0x3dcccccd, v233
	v_fma_f32 v80, s48, v152, v79
	global_store_dword v232, v80, s[18:19]
	v_add_u32_e32 v232, 0x1000, v232
	global_store_dword v235, v152, s[44:45]
	v_add_u32_e32 v235, 0x1000, v235
	global_store_dword v236, v80, s[46:47]
	v_add_u32_e32 v236, 0x1000, v236
	v_fma_f32 v233, -v80, v131, v81
	v_fmac_f32_e32 v152, 0x3dcccccd, v233
	v_fma_f32 v81, s48, v152, v80
	global_store_dword v232, v81, s[18:19]
	v_add_u32_e32 v232, 0x1000, v232
	global_store_dword v235, v152, s[44:45]
	v_add_u32_e32 v235, 0x1000, v235
	global_store_dword v236, v81, s[46:47]
	v_add_u32_e32 v236, 0x1000, v236
	v_add_u32_e32 v232, 0x80, v237
	v_mov_b32_e32 v235, v232
	v_mov_b32_e32 v236, v232
	v_fma_f32 v233, -v230, v1, v50
	v_fmac_f32_e32 v228, 0x3dcccccd, v233
	v_fma_f32 v50, s48, v228, v230
	global_store_dword v232, v50, s[18:19]
	v_add_u32_e32 v232, 0x1000, v232
	global_store_dword v235, v228, s[44:45]
	v_add_u32_e32 v235, 0x1000, v235
	global_store_dword v236, v50, s[46:47]
	v_add_u32_e32 v236, 0x1000, v236
	v_fma_f32 v233, -v50, v1, v51
	v_fmac_f32_e32 v228, 0x3dcccccd, v233
	v_fma_f32 v51, s48, v228, v50
	global_store_dword v232, v51, s[18:19]
	v_add_u32_e32 v232, 0x1000, v232
	global_store_dword v235, v228, s[44:45]
	v_add_u32_e32 v235, 0x1000, v235
	global_store_dword v236, v51, s[46:47]
	v_add_u32_e32 v236, 0x1000, v236
	v_fma_f32 v233, -v51, v1, v52
	v_fmac_f32_e32 v228, 0x3dcccccd, v233
	v_fma_f32 v52, s48, v228, v51
	global_store_dword v232, v52, s[18:19]
	v_add_u32_e32 v232, 0x1000, v232
	global_store_dword v235, v228, s[44:45]
	v_add_u32_e32 v235, 0x1000, v235
	global_store_dword v236, v52, s[46:47]
	v_add_u32_e32 v236, 0x1000, v236
	v_fma_f32 v233, -v52, v1, v53
	v_fmac_f32_e32 v228, 0x3dcccccd, v233
	v_fma_f32 v53, s48, v228, v52
	global_store_dword v232, v53, s[18:19]
	v_add_u32_e32 v232, 0x1000, v232
	global_store_dword v235, v228, s[44:45]
	v_add_u32_e32 v235, 0x1000, v235
	global_store_dword v236, v53, s[46:47]
	v_add_u32_e32 v236, 0x1000, v236
	v_fma_f32 v233, -v53, v1, v54
	v_fmac_f32_e32 v228, 0x3dcccccd, v233
	v_fma_f32 v54, s48, v228, v53
	global_store_dword v232, v54, s[18:19]
	v_add_u32_e32 v232, 0x1000, v232
	global_store_dword v235, v228, s[44:45]
	v_add_u32_e32 v235, 0x1000, v235
	global_store_dword v236, v54, s[46:47]
	v_add_u32_e32 v236, 0x1000, v236
	v_fma_f32 v233, -v54, v1, v55
	v_fmac_f32_e32 v228, 0x3dcccccd, v233
	v_fma_f32 v55, s48, v228, v54
	global_store_dword v232, v55, s[18:19]
	v_add_u32_e32 v232, 0x1000, v232
	global_store_dword v235, v228, s[44:45]
	v_add_u32_e32 v235, 0x1000, v235
	global_store_dword v236, v55, s[46:47]
	v_add_u32_e32 v236, 0x1000, v236
	v_fma_f32 v233, -v55, v1, v56
	v_fmac_f32_e32 v228, 0x3dcccccd, v233
	v_fma_f32 v56, s48, v228, v55
	global_store_dword v232, v56, s[18:19]
	v_add_u32_e32 v232, 0x1000, v232
	global_store_dword v235, v228, s[44:45]
	v_add_u32_e32 v235, 0x1000, v235
	global_store_dword v236, v56, s[46:47]
	v_add_u32_e32 v236, 0x1000, v236
	v_fma_f32 v233, -v56, v1, v57
	v_fmac_f32_e32 v228, 0x3dcccccd, v233
	v_fma_f32 v57, s48, v228, v56
	global_store_dword v232, v57, s[18:19]
	v_add_u32_e32 v232, 0x1000, v232
	global_store_dword v235, v228, s[44:45]
	v_add_u32_e32 v235, 0x1000, v235
	global_store_dword v236, v57, s[46:47]
	v_add_u32_e32 v236, 0x1000, v236
	v_fma_f32 v233, -v57, v1, v58
	v_fmac_f32_e32 v228, 0x3dcccccd, v233
	v_fma_f32 v58, s48, v228, v57
	global_store_dword v232, v58, s[18:19]
	v_add_u32_e32 v232, 0x1000, v232
	global_store_dword v235, v228, s[44:45]
	v_add_u32_e32 v235, 0x1000, v235
	global_store_dword v236, v58, s[46:47]
	v_add_u32_e32 v236, 0x1000, v236
	v_fma_f32 v233, -v58, v1, v59
	v_fmac_f32_e32 v228, 0x3dcccccd, v233
	v_fma_f32 v59, s48, v228, v58
	global_store_dword v232, v59, s[18:19]
	v_add_u32_e32 v232, 0x1000, v232
	global_store_dword v235, v228, s[44:45]
	v_add_u32_e32 v235, 0x1000, v235
	global_store_dword v236, v59, s[46:47]
	v_add_u32_e32 v236, 0x1000, v236
	v_fma_f32 v233, -v59, v1, v60
	v_fmac_f32_e32 v228, 0x3dcccccd, v233
	v_fma_f32 v60, s48, v228, v59
	global_store_dword v232, v60, s[18:19]
	v_add_u32_e32 v232, 0x1000, v232
	global_store_dword v235, v228, s[44:45]
	v_add_u32_e32 v235, 0x1000, v235
	global_store_dword v236, v60, s[46:47]
	v_add_u32_e32 v236, 0x1000, v236
	v_fma_f32 v233, -v60, v1, v61
	v_fmac_f32_e32 v228, 0x3dcccccd, v233
	v_fma_f32 v61, s48, v228, v60
	global_store_dword v232, v61, s[18:19]
	v_add_u32_e32 v232, 0x1000, v232
	global_store_dword v235, v228, s[44:45]
	v_add_u32_e32 v235, 0x1000, v235
	global_store_dword v236, v61, s[46:47]
	v_add_u32_e32 v236, 0x1000, v236
	v_fma_f32 v233, -v61, v1, v62
	v_fmac_f32_e32 v228, 0x3dcccccd, v233
	v_fma_f32 v62, s48, v228, v61
	global_store_dword v232, v62, s[18:19]
	v_add_u32_e32 v232, 0x1000, v232
	global_store_dword v235, v228, s[44:45]
	v_add_u32_e32 v235, 0x1000, v235
	global_store_dword v236, v62, s[46:47]
	v_add_u32_e32 v236, 0x1000, v236
	v_fma_f32 v233, -v62, v1, v63
	v_fmac_f32_e32 v228, 0x3dcccccd, v233
	v_fma_f32 v63, s48, v228, v62
	global_store_dword v232, v63, s[18:19]
	v_add_u32_e32 v232, 0x1000, v232
	global_store_dword v235, v228, s[44:45]
	v_add_u32_e32 v235, 0x1000, v235
	global_store_dword v236, v63, s[46:47]
	v_add_u32_e32 v236, 0x1000, v236
	v_fma_f32 v233, -v63, v1, v64
	v_fmac_f32_e32 v228, 0x3dcccccd, v233
	v_fma_f32 v64, s48, v228, v63
	global_store_dword v232, v64, s[18:19]
	v_add_u32_e32 v232, 0x1000, v232
	global_store_dword v235, v228, s[44:45]
	v_add_u32_e32 v235, 0x1000, v235
	global_store_dword v236, v64, s[46:47]
	v_add_u32_e32 v236, 0x1000, v236
	v_fma_f32 v233, -v64, v1, v65
	v_fmac_f32_e32 v228, 0x3dcccccd, v233
	v_fma_f32 v65, s48, v228, v64
	global_store_dword v232, v65, s[18:19]
	v_add_u32_e32 v232, 0x1000, v232
	global_store_dword v235, v228, s[44:45]
	v_add_u32_e32 v235, 0x1000, v235
	global_store_dword v236, v65, s[46:47]
	v_add_u32_e32 v236, 0x1000, v236
	v_fma_f32 v233, -v65, v1, v34
	v_fmac_f32_e32 v228, 0x3dcccccd, v233
	v_fma_f32 v34, s48, v228, v65
	global_store_dword v232, v34, s[18:19]
	v_add_u32_e32 v232, 0x1000, v232
	global_store_dword v235, v228, s[44:45]
	v_add_u32_e32 v235, 0x1000, v235
	global_store_dword v236, v34, s[46:47]
	v_add_u32_e32 v236, 0x1000, v236
	v_fma_f32 v233, -v34, v1, v35
	v_fmac_f32_e32 v228, 0x3dcccccd, v233
	v_fma_f32 v35, s48, v228, v34
	global_store_dword v232, v35, s[18:19]
	v_add_u32_e32 v232, 0x1000, v232
	global_store_dword v235, v228, s[44:45]
	v_add_u32_e32 v235, 0x1000, v235
	global_store_dword v236, v35, s[46:47]
	v_add_u32_e32 v236, 0x1000, v236
	v_fma_f32 v233, -v35, v1, v36
	v_fmac_f32_e32 v228, 0x3dcccccd, v233
	v_fma_f32 v36, s48, v228, v35
	global_store_dword v232, v36, s[18:19]
	v_add_u32_e32 v232, 0x1000, v232
	global_store_dword v235, v228, s[44:45]
	v_add_u32_e32 v235, 0x1000, v235
	global_store_dword v236, v36, s[46:47]
	v_add_u32_e32 v236, 0x1000, v236
	v_fma_f32 v233, -v36, v1, v37
	v_fmac_f32_e32 v228, 0x3dcccccd, v233
	v_fma_f32 v37, s48, v228, v36
	global_store_dword v232, v37, s[18:19]
	v_add_u32_e32 v232, 0x1000, v232
	global_store_dword v235, v228, s[44:45]
	v_add_u32_e32 v235, 0x1000, v235
	global_store_dword v236, v37, s[46:47]
	v_add_u32_e32 v236, 0x1000, v236
	v_fma_f32 v233, -v37, v1, v38
	v_fmac_f32_e32 v228, 0x3dcccccd, v233
	v_fma_f32 v38, s48, v228, v37
	global_store_dword v232, v38, s[18:19]
	v_add_u32_e32 v232, 0x1000, v232
	global_store_dword v235, v228, s[44:45]
	v_add_u32_e32 v235, 0x1000, v235
	global_store_dword v236, v38, s[46:47]
	v_add_u32_e32 v236, 0x1000, v236
	v_fma_f32 v233, -v38, v1, v39
	v_fmac_f32_e32 v228, 0x3dcccccd, v233
	v_fma_f32 v39, s48, v228, v38
	global_store_dword v232, v39, s[18:19]
	v_add_u32_e32 v232, 0x1000, v232
	global_store_dword v235, v228, s[44:45]
	v_add_u32_e32 v235, 0x1000, v235
	global_store_dword v236, v39, s[46:47]
	v_add_u32_e32 v236, 0x1000, v236
	v_fma_f32 v233, -v39, v1, v40
	v_fmac_f32_e32 v228, 0x3dcccccd, v233
	v_fma_f32 v40, s48, v228, v39
	global_store_dword v232, v40, s[18:19]
	v_add_u32_e32 v232, 0x1000, v232
	global_store_dword v235, v228, s[44:45]
	v_add_u32_e32 v235, 0x1000, v235
	global_store_dword v236, v40, s[46:47]
	v_add_u32_e32 v236, 0x1000, v236
	v_fma_f32 v233, -v40, v1, v41
	v_fmac_f32_e32 v228, 0x3dcccccd, v233
	v_fma_f32 v41, s48, v228, v40
	global_store_dword v232, v41, s[18:19]
	v_add_u32_e32 v232, 0x1000, v232
	global_store_dword v235, v228, s[44:45]
	v_add_u32_e32 v235, 0x1000, v235
	global_store_dword v236, v41, s[46:47]
	v_add_u32_e32 v236, 0x1000, v236
	v_fma_f32 v233, -v41, v1, v42
	v_fmac_f32_e32 v228, 0x3dcccccd, v233
	v_fma_f32 v42, s48, v228, v41
	global_store_dword v232, v42, s[18:19]
	v_add_u32_e32 v232, 0x1000, v232
	global_store_dword v235, v228, s[44:45]
	v_add_u32_e32 v235, 0x1000, v235
	global_store_dword v236, v42, s[46:47]
	v_add_u32_e32 v236, 0x1000, v236
	v_fma_f32 v233, -v42, v1, v43
	v_fmac_f32_e32 v228, 0x3dcccccd, v233
	v_fma_f32 v43, s48, v228, v42
	global_store_dword v232, v43, s[18:19]
	v_add_u32_e32 v232, 0x1000, v232
	global_store_dword v235, v228, s[44:45]
	v_add_u32_e32 v235, 0x1000, v235
	global_store_dword v236, v43, s[46:47]
	v_add_u32_e32 v236, 0x1000, v236
	v_fma_f32 v233, -v43, v1, v44
	v_fmac_f32_e32 v228, 0x3dcccccd, v233
	v_fma_f32 v44, s48, v228, v43
	global_store_dword v232, v44, s[18:19]
	v_add_u32_e32 v232, 0x1000, v232
	global_store_dword v235, v228, s[44:45]
	v_add_u32_e32 v235, 0x1000, v235
	global_store_dword v236, v44, s[46:47]
	v_add_u32_e32 v236, 0x1000, v236
	v_fma_f32 v233, -v44, v1, v45
	v_fmac_f32_e32 v228, 0x3dcccccd, v233
	v_fma_f32 v45, s48, v228, v44
	global_store_dword v232, v45, s[18:19]
	v_add_u32_e32 v232, 0x1000, v232
	global_store_dword v235, v228, s[44:45]
	v_add_u32_e32 v235, 0x1000, v235
	global_store_dword v236, v45, s[46:47]
	v_add_u32_e32 v236, 0x1000, v236
	v_fma_f32 v233, -v45, v1, v46
	v_fmac_f32_e32 v228, 0x3dcccccd, v233
	v_fma_f32 v46, s48, v228, v45
	global_store_dword v232, v46, s[18:19]
	v_add_u32_e32 v232, 0x1000, v232
	global_store_dword v235, v228, s[44:45]
	v_add_u32_e32 v235, 0x1000, v235
	global_store_dword v236, v46, s[46:47]
	v_add_u32_e32 v236, 0x1000, v236
	v_fma_f32 v233, -v46, v1, v47
	v_fmac_f32_e32 v228, 0x3dcccccd, v233
	v_fma_f32 v47, s48, v228, v46
	global_store_dword v232, v47, s[18:19]
	v_add_u32_e32 v232, 0x1000, v232
	global_store_dword v235, v228, s[44:45]
	v_add_u32_e32 v235, 0x1000, v235
	global_store_dword v236, v47, s[46:47]
	v_add_u32_e32 v236, 0x1000, v236
	v_fma_f32 v233, -v47, v1, v48
	v_fmac_f32_e32 v228, 0x3dcccccd, v233
	v_fma_f32 v48, s48, v228, v47
	global_store_dword v232, v48, s[18:19]
	v_add_u32_e32 v232, 0x1000, v232
	global_store_dword v235, v228, s[44:45]
	v_add_u32_e32 v235, 0x1000, v235
	global_store_dword v236, v48, s[46:47]
	v_add_u32_e32 v236, 0x1000, v236
	v_fma_f32 v233, -v48, v1, v49
	v_fmac_f32_e32 v228, 0x3dcccccd, v233
	v_fma_f32 v49, s48, v228, v48
	global_store_dword v232, v49, s[18:19]
	v_add_u32_e32 v232, 0x1000, v232
	global_store_dword v235, v228, s[44:45]
	v_add_u32_e32 v235, 0x1000, v235
	global_store_dword v236, v49, s[46:47]
	v_add_u32_e32 v236, 0x1000, v236
	v_fma_f32 v233, -v49, v1, v18
	v_fmac_f32_e32 v228, 0x3dcccccd, v233
	v_fma_f32 v18, s48, v228, v49
	global_store_dword v232, v18, s[18:19]
	v_add_u32_e32 v232, 0x1000, v232
	global_store_dword v235, v228, s[44:45]
	v_add_u32_e32 v235, 0x1000, v235
	global_store_dword v236, v18, s[46:47]
	v_add_u32_e32 v236, 0x1000, v236
	v_fma_f32 v233, -v18, v1, v19
	v_fmac_f32_e32 v228, 0x3dcccccd, v233
	v_fma_f32 v19, s48, v228, v18
	global_store_dword v232, v19, s[18:19]
	v_add_u32_e32 v232, 0x1000, v232
	global_store_dword v235, v228, s[44:45]
	v_add_u32_e32 v235, 0x1000, v235
	global_store_dword v236, v19, s[46:47]
	v_add_u32_e32 v236, 0x1000, v236
	v_fma_f32 v233, -v19, v1, v20
	v_fmac_f32_e32 v228, 0x3dcccccd, v233
	v_fma_f32 v20, s48, v228, v19
	global_store_dword v232, v20, s[18:19]
	v_add_u32_e32 v232, 0x1000, v232
	global_store_dword v235, v228, s[44:45]
	v_add_u32_e32 v235, 0x1000, v235
	global_store_dword v236, v20, s[46:47]
	v_add_u32_e32 v236, 0x1000, v236
	v_fma_f32 v233, -v20, v1, v21
	v_fmac_f32_e32 v228, 0x3dcccccd, v233
	v_fma_f32 v21, s48, v228, v20
	global_store_dword v232, v21, s[18:19]
	v_add_u32_e32 v232, 0x1000, v232
	global_store_dword v235, v228, s[44:45]
	v_add_u32_e32 v235, 0x1000, v235
	global_store_dword v236, v21, s[46:47]
	v_add_u32_e32 v236, 0x1000, v236
	v_fma_f32 v233, -v21, v1, v22
	v_fmac_f32_e32 v228, 0x3dcccccd, v233
	v_fma_f32 v22, s48, v228, v21
	global_store_dword v232, v22, s[18:19]
	v_add_u32_e32 v232, 0x1000, v232
	global_store_dword v235, v228, s[44:45]
	v_add_u32_e32 v235, 0x1000, v235
	global_store_dword v236, v22, s[46:47]
	v_add_u32_e32 v236, 0x1000, v236
	v_fma_f32 v233, -v22, v1, v23
	v_fmac_f32_e32 v228, 0x3dcccccd, v233
	v_fma_f32 v23, s48, v228, v22
	global_store_dword v232, v23, s[18:19]
	v_add_u32_e32 v232, 0x1000, v232
	global_store_dword v235, v228, s[44:45]
	v_add_u32_e32 v235, 0x1000, v235
	global_store_dword v236, v23, s[46:47]
	v_add_u32_e32 v236, 0x1000, v236
	v_fma_f32 v233, -v23, v1, v24
	v_fmac_f32_e32 v228, 0x3dcccccd, v233
	v_fma_f32 v24, s48, v228, v23
	global_store_dword v232, v24, s[18:19]
	v_add_u32_e32 v232, 0x1000, v232
	global_store_dword v235, v228, s[44:45]
	v_add_u32_e32 v235, 0x1000, v235
	global_store_dword v236, v24, s[46:47]
	v_add_u32_e32 v236, 0x1000, v236
	v_fma_f32 v233, -v24, v1, v25
	v_fmac_f32_e32 v228, 0x3dcccccd, v233
	v_fma_f32 v25, s48, v228, v24
	global_store_dword v232, v25, s[18:19]
	v_add_u32_e32 v232, 0x1000, v232
	global_store_dword v235, v228, s[44:45]
	v_add_u32_e32 v235, 0x1000, v235
	global_store_dword v236, v25, s[46:47]
	v_add_u32_e32 v236, 0x1000, v236
	v_fma_f32 v233, -v25, v1, v26
	v_fmac_f32_e32 v228, 0x3dcccccd, v233
	v_fma_f32 v26, s48, v228, v25
	global_store_dword v232, v26, s[18:19]
	v_add_u32_e32 v232, 0x1000, v232
	global_store_dword v235, v228, s[44:45]
	v_add_u32_e32 v235, 0x1000, v235
	global_store_dword v236, v26, s[46:47]
	v_add_u32_e32 v236, 0x1000, v236
	v_fma_f32 v233, -v26, v1, v27
	v_fmac_f32_e32 v228, 0x3dcccccd, v233
	v_fma_f32 v27, s48, v228, v26
	global_store_dword v232, v27, s[18:19]
	v_add_u32_e32 v232, 0x1000, v232
	global_store_dword v235, v228, s[44:45]
	v_add_u32_e32 v235, 0x1000, v235
	global_store_dword v236, v27, s[46:47]
	v_add_u32_e32 v236, 0x1000, v236
	v_fma_f32 v233, -v27, v1, v28
	v_fmac_f32_e32 v228, 0x3dcccccd, v233
	v_fma_f32 v28, s48, v228, v27
	global_store_dword v232, v28, s[18:19]
	v_add_u32_e32 v232, 0x1000, v232
	global_store_dword v235, v228, s[44:45]
	v_add_u32_e32 v235, 0x1000, v235
	global_store_dword v236, v28, s[46:47]
	v_add_u32_e32 v236, 0x1000, v236
	v_fma_f32 v233, -v28, v1, v29
	v_fmac_f32_e32 v228, 0x3dcccccd, v233
	v_fma_f32 v29, s48, v228, v28
	global_store_dword v232, v29, s[18:19]
	v_add_u32_e32 v232, 0x1000, v232
	global_store_dword v235, v228, s[44:45]
	v_add_u32_e32 v235, 0x1000, v235
	global_store_dword v236, v29, s[46:47]
	v_add_u32_e32 v236, 0x1000, v236
	v_fma_f32 v233, -v29, v1, v30
	v_fmac_f32_e32 v228, 0x3dcccccd, v233
	v_fma_f32 v30, s48, v228, v29
	global_store_dword v232, v30, s[18:19]
	v_add_u32_e32 v232, 0x1000, v232
	global_store_dword v235, v228, s[44:45]
	v_add_u32_e32 v235, 0x1000, v235
	global_store_dword v236, v30, s[46:47]
	v_add_u32_e32 v236, 0x1000, v236
	v_fma_f32 v233, -v30, v1, v31
	v_fmac_f32_e32 v228, 0x3dcccccd, v233
	v_fma_f32 v31, s48, v228, v30
	global_store_dword v232, v31, s[18:19]
	v_add_u32_e32 v232, 0x1000, v232
	global_store_dword v235, v228, s[44:45]
	v_add_u32_e32 v235, 0x1000, v235
	global_store_dword v236, v31, s[46:47]
	v_add_u32_e32 v236, 0x1000, v236
	v_fma_f32 v233, -v31, v1, v32
	v_fmac_f32_e32 v228, 0x3dcccccd, v233
	v_fma_f32 v32, s48, v228, v31
	global_store_dword v232, v32, s[18:19]
	v_add_u32_e32 v232, 0x1000, v232
	global_store_dword v235, v228, s[44:45]
	v_add_u32_e32 v235, 0x1000, v235
	global_store_dword v236, v32, s[46:47]
	v_add_u32_e32 v236, 0x1000, v236
	v_fma_f32 v233, -v32, v1, v33
	v_fmac_f32_e32 v228, 0x3dcccccd, v233
	v_fma_f32 v33, s48, v228, v32
	global_store_dword v232, v33, s[18:19]
	v_add_u32_e32 v232, 0x1000, v232
	global_store_dword v235, v228, s[44:45]
	v_add_u32_e32 v235, 0x1000, v235
	global_store_dword v236, v33, s[46:47]
	v_add_u32_e32 v236, 0x1000, v236
	v_fma_f32 v233, -v33, v1, v2
	v_fmac_f32_e32 v228, 0x3dcccccd, v233
	v_fma_f32 v2, s48, v228, v33
	global_store_dword v232, v2, s[18:19]
	v_add_u32_e32 v232, 0x1000, v232
	global_store_dword v235, v228, s[44:45]
	v_add_u32_e32 v235, 0x1000, v235
	global_store_dword v236, v2, s[46:47]
	v_add_u32_e32 v236, 0x1000, v236
	v_fma_f32 v233, -v2, v1, v3
	v_fmac_f32_e32 v228, 0x3dcccccd, v233
	v_fma_f32 v3, s48, v228, v2
	global_store_dword v232, v3, s[18:19]
	v_add_u32_e32 v232, 0x1000, v232
	global_store_dword v235, v228, s[44:45]
	v_add_u32_e32 v235, 0x1000, v235
	global_store_dword v236, v3, s[46:47]
	v_add_u32_e32 v236, 0x1000, v236
	v_fma_f32 v233, -v3, v1, v4
	v_fmac_f32_e32 v228, 0x3dcccccd, v233
	v_fma_f32 v4, s48, v228, v3
	global_store_dword v232, v4, s[18:19]
	v_add_u32_e32 v232, 0x1000, v232
	global_store_dword v235, v228, s[44:45]
	v_add_u32_e32 v235, 0x1000, v235
	global_store_dword v236, v4, s[46:47]
	v_add_u32_e32 v236, 0x1000, v236
	v_fma_f32 v233, -v4, v1, v5
	v_fmac_f32_e32 v228, 0x3dcccccd, v233
	v_fma_f32 v5, s48, v228, v4
	global_store_dword v232, v5, s[18:19]
	v_add_u32_e32 v232, 0x1000, v232
	global_store_dword v235, v228, s[44:45]
	v_add_u32_e32 v235, 0x1000, v235
	global_store_dword v236, v5, s[46:47]
	v_add_u32_e32 v236, 0x1000, v236
	v_fma_f32 v233, -v5, v1, v6
	v_fmac_f32_e32 v228, 0x3dcccccd, v233
	v_fma_f32 v6, s48, v228, v5
	global_store_dword v232, v6, s[18:19]
	v_add_u32_e32 v232, 0x1000, v232
	global_store_dword v235, v228, s[44:45]
	v_add_u32_e32 v235, 0x1000, v235
	global_store_dword v236, v6, s[46:47]
	v_add_u32_e32 v236, 0x1000, v236
	v_fma_f32 v233, -v6, v1, v7
	v_fmac_f32_e32 v228, 0x3dcccccd, v233
	v_fma_f32 v7, s48, v228, v6
	global_store_dword v232, v7, s[18:19]
	v_add_u32_e32 v232, 0x1000, v232
	global_store_dword v235, v228, s[44:45]
	v_add_u32_e32 v235, 0x1000, v235
	global_store_dword v236, v7, s[46:47]
	v_add_u32_e32 v236, 0x1000, v236
	v_fma_f32 v233, -v7, v1, v8
	v_fmac_f32_e32 v228, 0x3dcccccd, v233
	v_fma_f32 v8, s48, v228, v7
	global_store_dword v232, v8, s[18:19]
	v_add_u32_e32 v232, 0x1000, v232
	global_store_dword v235, v228, s[44:45]
	v_add_u32_e32 v235, 0x1000, v235
	global_store_dword v236, v8, s[46:47]
	v_add_u32_e32 v236, 0x1000, v236
	v_fma_f32 v233, -v8, v1, v9
	v_fmac_f32_e32 v228, 0x3dcccccd, v233
	v_fma_f32 v9, s48, v228, v8
	global_store_dword v232, v9, s[18:19]
	v_add_u32_e32 v232, 0x1000, v232
	global_store_dword v235, v228, s[44:45]
	v_add_u32_e32 v235, 0x1000, v235
	global_store_dword v236, v9, s[46:47]
	v_add_u32_e32 v236, 0x1000, v236
	v_fma_f32 v233, -v9, v1, v10
	v_fmac_f32_e32 v228, 0x3dcccccd, v233
	v_fma_f32 v10, s48, v228, v9
	global_store_dword v232, v10, s[18:19]
	v_add_u32_e32 v232, 0x1000, v232
	global_store_dword v235, v228, s[44:45]
	v_add_u32_e32 v235, 0x1000, v235
	global_store_dword v236, v10, s[46:47]
	v_add_u32_e32 v236, 0x1000, v236
	v_fma_f32 v233, -v10, v1, v11
	v_fmac_f32_e32 v228, 0x3dcccccd, v233
	v_fma_f32 v11, s48, v228, v10
	global_store_dword v232, v11, s[18:19]
	v_add_u32_e32 v232, 0x1000, v232
	global_store_dword v235, v228, s[44:45]
	v_add_u32_e32 v235, 0x1000, v235
	global_store_dword v236, v11, s[46:47]
	v_add_u32_e32 v236, 0x1000, v236
	v_fma_f32 v233, -v11, v1, v12
	v_fmac_f32_e32 v228, 0x3dcccccd, v233
	v_fma_f32 v12, s48, v228, v11
	global_store_dword v232, v12, s[18:19]
	v_add_u32_e32 v232, 0x1000, v232
	global_store_dword v235, v228, s[44:45]
	v_add_u32_e32 v235, 0x1000, v235
	global_store_dword v236, v12, s[46:47]
	v_add_u32_e32 v236, 0x1000, v236
	v_fma_f32 v233, -v12, v1, v13
	v_fmac_f32_e32 v228, 0x3dcccccd, v233
	v_fma_f32 v13, s48, v228, v12
	global_store_dword v232, v13, s[18:19]
	v_add_u32_e32 v232, 0x1000, v232
	global_store_dword v235, v228, s[44:45]
	v_add_u32_e32 v235, 0x1000, v235
	global_store_dword v236, v13, s[46:47]
	v_add_u32_e32 v236, 0x1000, v236
	v_fma_f32 v233, -v13, v1, v14
	v_fmac_f32_e32 v228, 0x3dcccccd, v233
	v_fma_f32 v14, s48, v228, v13
	global_store_dword v232, v14, s[18:19]
	v_add_u32_e32 v232, 0x1000, v232
	global_store_dword v235, v228, s[44:45]
	v_add_u32_e32 v235, 0x1000, v235
	global_store_dword v236, v14, s[46:47]
	v_add_u32_e32 v236, 0x1000, v236
	v_fma_f32 v233, -v14, v1, v15
	v_fmac_f32_e32 v228, 0x3dcccccd, v233
	v_fma_f32 v15, s48, v228, v14
	global_store_dword v232, v15, s[18:19]
	v_add_u32_e32 v232, 0x1000, v232
	global_store_dword v235, v228, s[44:45]
	v_add_u32_e32 v235, 0x1000, v235
	global_store_dword v236, v15, s[46:47]
	v_add_u32_e32 v236, 0x1000, v236
	v_fma_f32 v233, -v15, v1, v16
	v_fmac_f32_e32 v228, 0x3dcccccd, v233
	v_fma_f32 v16, s48, v228, v15
	global_store_dword v232, v16, s[18:19]
	v_add_u32_e32 v232, 0x1000, v232
	global_store_dword v235, v228, s[44:45]
	v_add_u32_e32 v235, 0x1000, v235
	global_store_dword v236, v16, s[46:47]
	v_add_u32_e32 v236, 0x1000, v236
	v_fma_f32 v233, -v16, v1, v17
	v_fmac_f32_e32 v228, 0x3dcccccd, v233
	v_fma_f32 v17, s48, v228, v16
	global_store_dword v232, v17, s[18:19]
	v_add_u32_e32 v232, 0x1000, v232
	global_store_dword v235, v228, s[44:45]
	v_add_u32_e32 v235, 0x1000, v235
	global_store_dword v236, v17, s[46:47]
	v_add_u32_e32 v236, 0x1000, v236
	s_endpgm
